# final stack with the MoE stagger split by waves 4-7 (SIMD-sharing pairs) instead of odd waves
# speedup vs baseline: 1.0057x; 1.0004x over previous
.LBB0_1013:
	s_or_b64 exec, exec, s[34:35]
	s_waitcnt vmcnt(0)
	v_lshlrev_b32_e32 v3, 11, v3
	v_and_b32_e32 v3, 0x7fff800, v3
	s_lshl_b64 s[34:35], s[10:11], 22
	s_add_u32 s10, s12, s34
	s_addc_u32 s52, s13, s35
	s_lshl_b32 s34, s36, 9
	s_lshl_b32 s35, s46, 6
	s_sub_i32 s34, s35, s34
	s_ashr_i32 s35, s34, 31
	s_lshl_b64 s[36:37], s[34:35], 2
	s_add_u32 s36, s10, s36
	s_addc_u32 s37, s52, s37
	v_or_b32_e32 v146, v3, v1
	s_waitcnt lgkmcnt(0)
	v_readfirstlane_b32 s51, v2
	v_lshl_add_u64 v[2:3], s[36:37], 0, v[152:153]
	v_lshl_add_u64 v[156:157], v[2:3], 0, v[148:149]
	s_mov_b64 s[36:37], -1
	s_cmp_ge_i32 s38, s50
	v_lshl_add_u64 v[132:133], v[156:157], 0, s[22:23]
	v_lshl_add_u64 v[130:131], v[156:157], 0, s[24:25]
	v_lshl_add_u64 v[134:135], v[156:157], 0, s[26:27]
	v_lshl_add_u64 v[138:139], v[156:157], 0, s[28:29]
	v_lshl_add_u64 v[142:143], v[156:157], 0, s[30:31]
	s_cbranch_scc0 .LBB0_1017
	global_load_dwordx4 v[2:5], v[156:157], off sc1 nt
	s_mov_b32 m0, s39
	global_load_dwordx4 v[6:9], v[132:133], off sc1 nt
	v_lshl_add_u64 v[50:51], s[14:15], 0, v[146:147]
	global_load_lds_dwordx4 v146, s[14:15]
	global_load_dwordx4 v[34:37], v[130:131], off sc1 nt
	global_load_dwordx4 v[38:41], v[134:135], off sc1 nt
	s_mov_b32 m0, s40
	s_nop 0
	global_load_lds_dwordx4 v146, s[16:17]
	s_waitcnt vmcnt(4)
	s_nop 0
	v_cvt_pk_bf16_f32 v2, v2, v6
	ds_write_b32 v169, v2 offset:49152
	v_cvt_pk_bf16_f32 v2, v3, v7
	ds_write_b32 v169, v2 offset:49216
	v_cvt_pk_bf16_f32 v2, v4, v8
	ds_write_b32 v169, v2 offset:49280
	v_cvt_pk_bf16_f32 v2, v5, v9
	ds_write_b32 v169, v2 offset:49344
	global_load_dwordx4 v[42:45], v[138:139], off sc1 nt
	global_load_dwordx4 v[46:49], v[142:143], off sc1 nt
	s_waitcnt vmcnt(5)
	s_mov_b32 m0, s41
	s_waitcnt lgkmcnt(0)
	s_barrier
	global_load_lds_dwordx4 v146, s[18:19]
	v_mov_b32_e32 v2, 0
	s_mov_b32 s37, -2
	s_movk_i32 s36, 0x80
	v_mov_b32_e32 v3, v2
	v_mov_b32_e32 v4, v2
	v_mov_b32_e32 v5, v2
	v_mov_b32_e32 v6, v2
	v_mov_b32_e32 v7, v2
	v_mov_b32_e32 v8, v2
	v_mov_b32_e32 v9, v2
	v_mov_b32_e32 v10, v2
	v_mov_b32_e32 v11, v2
	v_mov_b32_e32 v12, v2
	v_mov_b32_e32 v13, v2
	v_mov_b32_e32 v14, v2
	v_mov_b32_e32 v15, v2
	v_mov_b32_e32 v16, v2
	v_mov_b32_e32 v17, v2
	v_mov_b32_e32 v66, v2
	v_mov_b32_e32 v67, v2
	v_mov_b32_e32 v68, v2
	v_mov_b32_e32 v69, v2
	v_mov_b32_e32 v70, v2
	v_mov_b32_e32 v71, v2
	v_mov_b32_e32 v72, v2
	v_mov_b32_e32 v73, v2
	v_mov_b32_e32 v74, v2
	v_mov_b32_e32 v75, v2
	v_mov_b32_e32 v76, v2
	v_mov_b32_e32 v77, v2
	v_mov_b32_e32 v78, v2
	v_mov_b32_e32 v79, v2
	v_mov_b32_e32 v80, v2
	v_mov_b32_e32 v81, v2
	v_mov_b32_e32 v18, v2
	v_mov_b32_e32 v19, v2
	v_mov_b32_e32 v20, v2
	v_mov_b32_e32 v21, v2
	v_mov_b32_e32 v22, v2
	v_mov_b32_e32 v23, v2
	v_mov_b32_e32 v24, v2
	v_mov_b32_e32 v25, v2
	v_mov_b32_e32 v26, v2
	v_mov_b32_e32 v27, v2
	v_mov_b32_e32 v28, v2
	v_mov_b32_e32 v29, v2
	v_mov_b32_e32 v30, v2
	v_mov_b32_e32 v31, v2
	v_mov_b32_e32 v32, v2
	v_mov_b32_e32 v33, v2
	v_mov_b32_e32 v114, v2
	v_mov_b32_e32 v115, v2
	v_mov_b32_e32 v116, v2
	v_mov_b32_e32 v117, v2
	v_mov_b32_e32 v118, v2
	v_mov_b32_e32 v119, v2
	v_mov_b32_e32 v120, v2
	v_mov_b32_e32 v121, v2
	v_mov_b32_e32 v122, v2
	v_mov_b32_e32 v123, v2
	v_mov_b32_e32 v124, v2
	v_mov_b32_e32 v125, v2
	v_mov_b32_e32 v126, v2
	v_mov_b32_e32 v127, v2
	v_mov_b32_e32 v128, v2
	v_mov_b32_e32 v129, v2
	v_readfirstlane_b32 s98, v250
	s_bitcmp1_b32 s98, 8
	s_cbranch_scc1 .Lmoe_B_1015

.Lp9pf_n1:
	s_or_b64 exec, exec, s[100:101]
	s_waitcnt vmcnt(4)
	s_nop 0
	v_cvt_pk_bf16_f32 v2, v2, v6
	ds_write_b32 v167, v2 offset:49152
	v_cvt_pk_bf16_f32 v2, v3, v7
	ds_write_b32 v167, v2 offset:49216
	v_cvt_pk_bf16_f32 v2, v4, v8
	ds_write_b32 v167, v2 offset:49280
	v_cvt_pk_bf16_f32 v2, v5, v9
	ds_write_b32 v167, v2 offset:49344
	global_load_dwordx4 v[74:77], v[138:139], off sc1 nt
	global_load_dwordx4 v[78:81], v[142:143], off sc1 nt
	s_waitcnt vmcnt(5)
	s_mov_b32 m0, s41
	s_waitcnt lgkmcnt(0)
	s_barrier
	global_load_lds_dwordx4 v146, s[16:17]
	v_mov_b32_e32 v2, 0
	s_mov_b32 s36, -2
	s_movk_i32 s35, 0x80
	v_mov_b32_e32 v3, v2
	v_mov_b32_e32 v4, v2
	v_mov_b32_e32 v5, v2
	v_mov_b32_e32 v6, v2
	v_mov_b32_e32 v7, v2
	v_mov_b32_e32 v8, v2
	v_mov_b32_e32 v9, v2
	v_mov_b32_e32 v10, v2
	v_mov_b32_e32 v11, v2
	v_mov_b32_e32 v12, v2
	v_mov_b32_e32 v13, v2
	v_mov_b32_e32 v14, v2
	v_mov_b32_e32 v15, v2
	v_mov_b32_e32 v16, v2
	v_mov_b32_e32 v17, v2
	v_mov_b32_e32 v18, v2
	v_mov_b32_e32 v19, v2
	v_mov_b32_e32 v20, v2
	v_mov_b32_e32 v21, v2
	v_mov_b32_e32 v22, v2
	v_mov_b32_e32 v23, v2
	v_mov_b32_e32 v24, v2
	v_mov_b32_e32 v25, v2
	v_mov_b32_e32 v26, v2
	v_mov_b32_e32 v27, v2
	v_mov_b32_e32 v28, v2
	v_mov_b32_e32 v29, v2
	v_mov_b32_e32 v30, v2
	v_mov_b32_e32 v31, v2
	v_mov_b32_e32 v32, v2
	v_mov_b32_e32 v33, v2
	v_mov_b32_e32 v34, v2
	v_mov_b32_e32 v35, v2
	v_mov_b32_e32 v36, v2
	v_mov_b32_e32 v37, v2
	v_mov_b32_e32 v38, v2
	v_mov_b32_e32 v39, v2
	v_mov_b32_e32 v40, v2
	v_mov_b32_e32 v41, v2
	v_mov_b32_e32 v42, v2
	v_mov_b32_e32 v43, v2
	v_mov_b32_e32 v44, v2
	v_mov_b32_e32 v45, v2
	v_mov_b32_e32 v46, v2
	v_mov_b32_e32 v47, v2
	v_mov_b32_e32 v48, v2
	v_mov_b32_e32 v49, v2
	v_mov_b32_e32 v50, v2
	v_mov_b32_e32 v51, v2
	v_mov_b32_e32 v52, v2
	v_mov_b32_e32 v53, v2
	v_mov_b32_e32 v54, v2
	v_mov_b32_e32 v55, v2
	v_mov_b32_e32 v56, v2
	v_mov_b32_e32 v57, v2
	v_mov_b32_e32 v58, v2
	v_mov_b32_e32 v59, v2
	v_mov_b32_e32 v60, v2
	v_mov_b32_e32 v61, v2
	v_mov_b32_e32 v62, v2
	v_mov_b32_e32 v63, v2
	v_mov_b32_e32 v64, v2
	v_mov_b32_e32 v65, v2
	v_readfirstlane_b32 s98, v250
	s_bitcmp1_b32 s98, 8
	s_cbranch_scc1 .Lmoe_B_1087

.Lp9pf_t1:
	s_or_b64 exec, exec, s[100:101]
	s_waitcnt vmcnt(6)
	s_nop 0
	v_cvt_pk_bf16_f32 v2, v2, v6
	ds_write_b32 v167, v2 offset:49152
	v_cvt_pk_bf16_f32 v2, v3, v7
	ds_write_b32 v167, v2 offset:49216
	v_cvt_pk_bf16_f32 v2, v4, v8
	ds_write_b32 v167, v2 offset:49280
	v_cvt_pk_bf16_f32 v2, v5, v9
	ds_write_b32 v167, v2 offset:49344
	global_load_dwordx4 v[138:141], v[138:139], off sc1 nt
	global_load_dwordx4 v[142:145], v[142:143], off sc1 nt
	s_waitcnt vmcnt(6)
	s_mov_b32 m0, s41
	s_waitcnt lgkmcnt(0)
	s_barrier
	global_load_lds_dwordx4 v146, s[16:17]
	s_mov_b32 m0, s44
	v_mov_b32_e32 v66, 0
	global_load_lds_dwordx4 v156, s[16:17]
	s_mov_b32 s36, -2
	s_movk_i32 s35, 0x80
	v_mov_b32_e32 v67, v66
	v_mov_b32_e32 v68, v66
	v_mov_b32_e32 v69, v66
	v_mov_b32_e32 v70, v66
	v_mov_b32_e32 v71, v66
	v_mov_b32_e32 v72, v66
	v_mov_b32_e32 v73, v66
	v_mov_b32_e32 v74, v66
	v_mov_b32_e32 v75, v66
	v_mov_b32_e32 v76, v66
	v_mov_b32_e32 v77, v66
	v_mov_b32_e32 v78, v66
	v_mov_b32_e32 v79, v66
	v_mov_b32_e32 v80, v66
	v_mov_b32_e32 v81, v66
	v_mov_b32_e32 v82, v66
	v_mov_b32_e32 v83, v66
	v_mov_b32_e32 v84, v66
	v_mov_b32_e32 v85, v66
	v_mov_b32_e32 v86, v66
	v_mov_b32_e32 v87, v66
	v_mov_b32_e32 v88, v66
	v_mov_b32_e32 v89, v66
	v_mov_b32_e32 v90, v66
	v_mov_b32_e32 v91, v66
	v_mov_b32_e32 v92, v66
	v_mov_b32_e32 v93, v66
	v_mov_b32_e32 v94, v66
	v_mov_b32_e32 v95, v66
	v_mov_b32_e32 v96, v66
	v_mov_b32_e32 v97, v66
	v_mov_b32_e32 v98, v66
	v_mov_b32_e32 v99, v66
	v_mov_b32_e32 v100, v66
	v_mov_b32_e32 v101, v66
	v_mov_b32_e32 v102, v66
	v_mov_b32_e32 v103, v66
	v_mov_b32_e32 v104, v66
	v_mov_b32_e32 v105, v66
	v_mov_b32_e32 v106, v66
	v_mov_b32_e32 v107, v66
	v_mov_b32_e32 v108, v66
	v_mov_b32_e32 v109, v66
	v_mov_b32_e32 v110, v66
	v_mov_b32_e32 v111, v66
	v_mov_b32_e32 v112, v66
	v_mov_b32_e32 v113, v66
	v_mov_b32_e32 v114, v66
	v_mov_b32_e32 v115, v66
	v_mov_b32_e32 v116, v66
	v_mov_b32_e32 v117, v66
	v_mov_b32_e32 v118, v66
	v_mov_b32_e32 v119, v66
	v_mov_b32_e32 v120, v66
	v_mov_b32_e32 v121, v66
	v_mov_b32_e32 v122, v66
	v_mov_b32_e32 v123, v66
	v_mov_b32_e32 v124, v66
	v_mov_b32_e32 v125, v66
	v_mov_b32_e32 v126, v66
	v_mov_b32_e32 v127, v66
	v_mov_b32_e32 v128, v66
	v_mov_b32_e32 v129, v66
	v_mov_b32_e32 v2, v66
	v_mov_b32_e32 v3, v66
	v_mov_b32_e32 v4, v66
	v_mov_b32_e32 v5, v66
	v_mov_b32_e32 v6, v66
	v_mov_b32_e32 v7, v66
	v_mov_b32_e32 v8, v66
	v_mov_b32_e32 v9, v66
	v_mov_b32_e32 v10, v66
	v_mov_b32_e32 v11, v66
	v_mov_b32_e32 v12, v66
	v_mov_b32_e32 v13, v66
	v_mov_b32_e32 v14, v66
	v_mov_b32_e32 v15, v66
	v_mov_b32_e32 v16, v66
	v_mov_b32_e32 v17, v66
	v_mov_b32_e32 v18, v66
	v_mov_b32_e32 v19, v66
	v_mov_b32_e32 v20, v66
	v_mov_b32_e32 v21, v66
	v_mov_b32_e32 v22, v66
	v_mov_b32_e32 v23, v66
	v_mov_b32_e32 v24, v66
	v_mov_b32_e32 v25, v66
	v_mov_b32_e32 v26, v66
	v_mov_b32_e32 v27, v66
	v_mov_b32_e32 v28, v66
	v_mov_b32_e32 v29, v66
	v_mov_b32_e32 v30, v66
	v_mov_b32_e32 v31, v66
	v_mov_b32_e32 v32, v66
	v_mov_b32_e32 v33, v66
	v_mov_b32_e32 v34, v66
	v_mov_b32_e32 v35, v66
	v_mov_b32_e32 v36, v66
	v_mov_b32_e32 v37, v66
	v_mov_b32_e32 v38, v66
	v_mov_b32_e32 v39, v66
	v_mov_b32_e32 v40, v66
	v_mov_b32_e32 v41, v66
	v_mov_b32_e32 v42, v66
	v_mov_b32_e32 v43, v66
	v_mov_b32_e32 v44, v66
	v_mov_b32_e32 v45, v66
	v_mov_b32_e32 v46, v66
	v_mov_b32_e32 v47, v66
	v_mov_b32_e32 v48, v66
	v_mov_b32_e32 v49, v66
	v_mov_b32_e32 v50, v66
	v_mov_b32_e32 v51, v66
	v_mov_b32_e32 v52, v66
	v_mov_b32_e32 v53, v66
	v_mov_b32_e32 v54, v66
	v_mov_b32_e32 v55, v66
	v_mov_b32_e32 v56, v66
	v_mov_b32_e32 v57, v66
	v_mov_b32_e32 v58, v66
	v_mov_b32_e32 v59, v66
	v_mov_b32_e32 v60, v66
	v_mov_b32_e32 v61, v66
	v_mov_b32_e32 v62, v66
	v_mov_b32_e32 v63, v66
	v_mov_b32_e32 v64, v66
	v_mov_b32_e32 v65, v66
	v_readfirstlane_b32 s98, v250
	s_bitcmp1_b32 s98, 8
	s_cbranch_scc1 .Lmoe_B_1091
